# moe2 next-unit set-up reuses the unit decode done under the K loop (no second binary search over the LDS tables)
# baseline (speedup 1.0000x reference)
;     __device__ __forceinline__ void mainloop(bfr* smem, const AL& al, const BL& bl) {
;     ...
;         } else if constexpr (MI == 3) {
; #pragma unroll
;             for (int kt = 0; kt < nk; kt += 6) {
;                 G_STEP3(0, 1, sa0, sb0, 2, 2);
;                 G_STEP3(1, 2, sa1, sb1, 0, 2);
;                 G_STEP3(2, 0, sa0, sb0, 1, 2);
;                 G_STEP3(3, 1, sa1, sb1, 2, 2);
;                 G_STEP3(4, 2, sa0, sb0, 0, 2);
;                 G_STEP3(5, 0, sa1, sb1, 1, 2);
;             }
.LBB0_1589:
	s_or_b64 exec, exec, s[12:13]
	v_add_co_u32_e32 v130, vcc, 0xe0000, v214
	s_nop 1
	v_addc_co_u32_e32 v131, vcc, 0, v215, vcc
	v_add_co_u32_e32 v134, vcc, 0xe1000, v214
	s_nop 1
	v_addc_co_u32_e32 v135, vcc, 0, v215, vcc
	v_add_co_u32_e32 v138, vcc, 0xe2000, v214
	global_load_dwordx4 v[130:133], v[130:131], off
	s_nop 0
	global_load_dwordx4 v[134:137], v[134:135], off
	v_addc_co_u32_e32 v139, vcc, 0, v215, vcc
	v_add_co_u32_e32 v142, vcc, 0xe3000, v214
	s_nop 1
	v_addc_co_u32_e32 v143, vcc, 0, v215, vcc
	global_load_dwordx4 v[138:141], v[138:139], off
	s_nop 0
	global_load_dwordx4 v[142:145], v[142:143], off
	v_mfma_f32_32x32x16_bf16 v[34:49], v[158:161], v[194:197], v[34:49]
	ds_read_b128 v[146:149], v219 offset:17968
	v_mfma_f32_32x32x16_bf16 v[18:33], v[162:165], v[186:189], v[18:33]
	ds_read_b64_tr_b16 v[178:179], v221
	ds_read_b64_tr_b16 v[180:181], v221 offset:2304
	v_mfma_f32_32x32x16_bf16 v[2:17], v[162:165], v[194:197], v[2:17]
	s_waitcnt lgkmcnt(10)
	v_mfma_f32_32x32x16_bf16 v[82:97], v[166:169], v[182:185], v[82:97]
	ds_read_b128 v[154:157], v219 offset:20528
	ds_read_b64_tr_b16 v[194:195], v222 offset:64
	ds_read_b64_tr_b16 v[196:197], v222 offset:2368
	s_waitcnt lgkmcnt(3)
	s_barrier
	s_waitcnt vmcnt(15)
	v_cmp_ne_u32_e32 vcc, 0, v251
	s_nop 1
	v_cndmask_b32_e32 v250, v250, v234, vcc
	v_max_i32_e32 v236, 0, v250
	v_mov_b32_e32 v237, 0
	v_lshl_add_u64 v[236:237], v[236:237], 2, s[10:11]
	global_load_dword v235, v[236:237], off
	v_mfma_f32_32x32x16_bf16 v[66:81], v[166:169], v[190:193], v[66:81]
	ds_read_b128 v[158:161], v219 offset:30736
	v_mfma_f32_32x32x16_bf16 v[50:65], v[170:173], v[182:185], v[50:65]
	v_mfma_f32_32x32x16_bf16 v[34:49], v[170:173], v[190:193], v[34:49]
	ds_read_b128 v[162:165], v219 offset:33296
	v_mfma_f32_32x32x16_bf16 v[18:33], v[174:177], v[182:185], v[18:33]
	ds_read_b64_tr_b16 v[182:183], v224
	ds_read_b64_tr_b16 v[184:185], v224 offset:2304
	v_mfma_f32_32x32x16_bf16 v[2:17], v[174:177], v[190:193], v[2:17]
	ds_read_b128 v[166:169], v219 offset:35856
	ds_read_b64_tr_b16 v[186:187], v224 offset:64
	ds_read_b64_tr_b16 v[188:189], v224 offset:2368
	v_mfma_f32_32x32x16_bf16 v[82:97], v[150:153], v[178:181], v[82:97]
	s_waitcnt vmcnt(10)
	ds_write_b128 v203, v[106:109] offset:16
	s_and_saveexec_b64 s[12:13], s[4:5]
	ds_write_b128 v216, v[98:101] offset:10256
	s_or_b64 exec, exec, s[12:13]
	s_waitcnt lgkmcnt(9)
	v_mfma_f32_32x32x16_bf16 v[66:81], v[150:153], v[194:197], v[66:81]
	ds_read_b128 v[170:173], v219 offset:30768
	s_waitcnt vmcnt(9)
	v_cvt_pk_bf16_f32 v150, v118, v119
	v_cvt_pk_bf16_f32 v151, v120, v121
	s_waitcnt vmcnt(8)
	v_cvt_pk_bf16_f32 v152, v110, v111
	v_cvt_pk_bf16_f32 v153, v112, v113
	ds_write2_b64 v198, v[150:151], v[152:153] offset0:130 offset1:202
	s_waitcnt vmcnt(7)
	v_cvt_pk_bf16_f32 v150, v114, v115
	v_cvt_pk_bf16_f32 v151, v116, v117
	s_waitcnt vmcnt(6)
	v_cvt_pk_bf16_f32 v152, v122, v123
	v_cvt_pk_bf16_f32 v153, v124, v125
	ds_write2_b64 v211, v[150:151], v[152:153] offset0:18 offset1:90
	v_mfma_f32_32x32x16_bf16 v[50:65], v[146:149], v[178:181], v[50:65]
	v_mfma_f32_32x32x16_bf16 v[34:49], v[146:149], v[194:197], v[34:49]
	ds_read_b128 v[174:177], v219 offset:33328
	v_mfma_f32_32x32x16_bf16 v[18:33], v[154:157], v[178:181], v[18:33]
	ds_read_b64_tr_b16 v[178:179], v225
	ds_read_b64_tr_b16 v[180:181], v225 offset:2304
	v_mfma_f32_32x32x16_bf16 v[2:17], v[154:157], v[194:197], v[2:17]
	s_waitcnt lgkmcnt(10)
	v_mfma_f32_32x32x16_bf16 v[82:97], v[158:161], v[182:185], v[82:97]
	ds_read_b128 v[190:193], v219 offset:35888
	ds_read_b64_tr_b16 v[194:195], v226 offset:64
	ds_read_b64_tr_b16 v[196:197], v226 offset:2368
	s_waitcnt lgkmcnt(3)
	s_barrier
; __device__ __forceinline__ void moe_unit(const int* pre, const int* lpre, int x, int lb, int& e, int& rb) {
;     if (lb < lpre[32]) {
;         int lo = 0, hi = 32;
;         while (hi - lo > 1) { const int mid = (lo + hi) >> 1; if (lpre[mid] <= lb) lo = mid; else hi = mid; }
;         e = x + 8 * lo; rb = lb - lpre[lo];
;     } else { e = 256; rb = (lb - lpre[32]) * 8 + x; }
; }
	v_mfma_f32_32x32x16_bf16 v[66:81], v[158:161], v[186:189], v[66:81]
	ds_read_b128 v[154:157], v219 offset:16
	v_mfma_f32_32x32x16_bf16 v[50:65], v[162:165], v[182:185], v[50:65]
	v_mfma_f32_32x32x16_bf16 v[34:49], v[162:165], v[186:189], v[34:49]
	ds_read_b128 v[158:161], v219 offset:2576
	v_mfma_f32_32x32x16_bf16 v[18:33], v[166:169], v[182:185], v[18:33]
	ds_read_b64_tr_b16 v[162:163], v227 offset:46096
	ds_read_b64_tr_b16 v[164:165], v227 offset:48400
	v_mfma_f32_32x32x16_bf16 v[2:17], v[166:169], v[186:189], v[2:17]
	ds_read_b128 v[146:149], v219 offset:5136
	ds_read_b64_tr_b16 v[150:151], v227 offset:46160
	ds_read_b64_tr_b16 v[152:153], v227 offset:48464
	v_mfma_f32_32x32x16_bf16 v[82:97], v[170:173], v[178:181], v[82:97]
	s_waitcnt vmcnt(5)
	ds_write_b128 v203, v[126:129] offset:15376
	s_and_saveexec_b64 s[12:13], s[4:5]
	ds_write_b128 v216, v[102:105] offset:25616
	s_or_b64 exec, exec, s[12:13]
	s_waitcnt lgkmcnt(9)
	v_mfma_f32_32x32x16_bf16 v[66:81], v[170:173], v[194:197], v[66:81]
	ds_read_b128 v[166:169], v219 offset:48
	s_waitcnt vmcnt(4)
	v_cvt_pk_bf16_f32 v170, v130, v131
	v_cvt_pk_bf16_f32 v171, v132, v133
	s_waitcnt vmcnt(3)
	v_cvt_pk_bf16_f32 v172, v134, v135
	v_cvt_pk_bf16_f32 v173, v136, v137
	ds_write2_b64 v218, v[170:171], v[172:173] offset1:72
	s_waitcnt vmcnt(2)
	v_cvt_pk_bf16_f32 v170, v138, v139
	v_cvt_pk_bf16_f32 v171, v140, v141
	s_waitcnt vmcnt(1)
	v_cvt_pk_bf16_f32 v172, v142, v143
	v_cvt_pk_bf16_f32 v173, v144, v145
	ds_write2_b64 v218, v[170:171], v[172:173] offset0:144 offset1:216
	v_mfma_f32_32x32x16_bf16 v[50:65], v[174:177], v[178:181], v[50:65]
	v_mfma_f32_32x32x16_bf16 v[34:49], v[174:177], v[194:197], v[34:49]
	ds_read_b128 v[170:173], v219 offset:2608
	v_mfma_f32_32x32x16_bf16 v[18:33], v[190:193], v[178:181], v[18:33]
	ds_read_b64_tr_b16 v[174:175], v227 offset:55312
	ds_read_b64_tr_b16 v[176:177], v227 offset:57616
	v_mfma_f32_32x32x16_bf16 v[2:17], v[190:193], v[194:197], v[2:17]
	s_waitcnt lgkmcnt(10)
	v_mfma_f32_32x32x16_bf16 v[82:97], v[154:157], v[162:165], v[82:97]
	ds_read_b128 v[178:181], v219 offset:5168
	ds_read_b64_tr_b16 v[182:183], v227 offset:55376
	ds_read_b64_tr_b16 v[184:185], v227 offset:57680
	s_waitcnt lgkmcnt(3)
	s_barrier
	v_mfma_f32_32x32x16_bf16 v[66:81], v[154:157], v[150:153], v[66:81]
	ds_read_b128 v[154:157], v219 offset:15376
	v_mfma_f32_32x32x16_bf16 v[50:65], v[158:161], v[162:165], v[50:65]
	v_mfma_f32_32x32x16_bf16 v[34:49], v[158:161], v[150:153], v[34:49]
	ds_read_b128 v[158:161], v219 offset:17936
	v_mfma_f32_32x32x16_bf16 v[18:33], v[146:149], v[162:165], v[18:33]
	ds_read_b64_tr_b16 v[162:163], v220
	ds_read_b64_tr_b16 v[164:165], v220 offset:2304
	v_mfma_f32_32x32x16_bf16 v[2:17], v[146:149], v[150:153], v[2:17]
	ds_read_b128 v[146:149], v219 offset:20496
	ds_read_b64_tr_b16 v[150:151], v220 offset:64
	ds_read_b64_tr_b16 v[152:153], v220 offset:2368
	v_mfma_f32_32x32x16_bf16 v[82:97], v[166:169], v[174:177], v[82:97]
	s_waitcnt lgkmcnt(7)
	v_mfma_f32_32x32x16_bf16 v[66:81], v[166:169], v[182:185], v[66:81]
	ds_read_b128 v[166:169], v219 offset:15408
	v_mfma_f32_32x32x16_bf16 v[50:65], v[170:173], v[174:177], v[50:65]
	v_mfma_f32_32x32x16_bf16 v[34:49], v[170:173], v[182:185], v[34:49]
	ds_read_b128 v[170:173], v219 offset:17968
	v_mfma_f32_32x32x16_bf16 v[18:33], v[178:181], v[174:177], v[18:33]
	ds_read_b64_tr_b16 v[174:175], v221
	ds_read_b64_tr_b16 v[176:177], v221 offset:2304
	v_mfma_f32_32x32x16_bf16 v[2:17], v[178:181], v[182:185], v[2:17]
	s_waitcnt lgkmcnt(7)
	v_mfma_f32_32x32x16_bf16 v[82:97], v[154:157], v[162:165], v[82:97]
	ds_read_b128 v[178:181], v219 offset:20528
	ds_read_b64_tr_b16 v[182:183], v222 offset:64
	ds_read_b64_tr_b16 v[184:185], v222 offset:2368
	s_waitcnt lgkmcnt(3)
	s_barrier
	v_mfma_f32_32x32x16_bf16 v[66:81], v[154:157], v[150:153], v[66:81]
	v_mfma_f32_32x32x16_bf16 v[50:65], v[158:161], v[162:165], v[50:65]
	v_mfma_f32_32x32x16_bf16 v[34:49], v[158:161], v[150:153], v[34:49]
	v_mfma_f32_32x32x16_bf16 v[18:33], v[146:149], v[162:165], v[18:33]
	v_mfma_f32_32x32x16_bf16 v[2:17], v[146:149], v[150:153], v[2:17]
	v_mfma_f32_32x32x16_bf16 v[82:97], v[166:169], v[174:177], v[82:97]
	s_waitcnt lgkmcnt(0)
	v_mfma_f32_32x32x16_bf16 v[66:81], v[166:169], v[182:185], v[66:81]
	v_mfma_f32_32x32x16_bf16 v[50:65], v[170:173], v[174:177], v[50:65]
	v_mfma_f32_32x32x16_bf16 v[34:49], v[170:173], v[182:185], v[34:49]
	v_mfma_f32_32x32x16_bf16 v[18:33], v[178:181], v[174:177], v[18:33]
	v_mfma_f32_32x32x16_bf16 v[2:17], v[178:181], v[182:185], v[2:17]
	s_add_i32 s23, s23, s27
	s_cmp_ge_i32 s23, s24
	s_cselect_b64 s[12:13], -1, 0
	s_and_b64 vcc, exec, s[12:13]
	s_barrier
	s_cbranch_vccnz .LBB0_1614
	s_mov_b32 s14, s68
	v_mov_b32_e32 v108, v238

;     __device__ __forceinline__ void mainloop(bfr* smem, const AL& al, const BL& bl) {
;     ...
;         } else if constexpr (MI == 3) {
; #pragma unroll
;             for (int kt = 0; kt < nk; kt += 6) {
;                 G_STEP3(0, 1, sa0, sb0, 2, 2);
;                 G_STEP3(1, 2, sa1, sb1, 0, 2);
;                 G_STEP3(2, 0, sa0, sb0, 1, 2);
;                 G_STEP3(3, 1, sa1, sb1, 2, 2);
;                 G_STEP3(4, 2, sa0, sb0, 0, 2);
;                 G_STEP3(5, 0, sa1, sb1, 1, 2);
;             }
.LBB0_2730:
	s_or_b64 exec, exec, s[12:13]
	v_add_co_u32_e32 v130, vcc, 0xe0000, v212
	s_nop 1
	v_addc_co_u32_e32 v131, vcc, 0, v213, vcc
	v_add_co_u32_e32 v134, vcc, 0xe1000, v212
	s_nop 1
	v_addc_co_u32_e32 v135, vcc, 0, v213, vcc
	v_add_co_u32_e32 v138, vcc, 0xe2000, v212
	global_load_dwordx4 v[130:133], v[130:131], off
	s_nop 0
	global_load_dwordx4 v[134:137], v[134:135], off
	v_addc_co_u32_e32 v139, vcc, 0, v213, vcc
	v_add_co_u32_e32 v142, vcc, 0xe3000, v212
	s_nop 1
	v_addc_co_u32_e32 v143, vcc, 0, v213, vcc
	global_load_dwordx4 v[138:141], v[138:139], off
	s_nop 0
	global_load_dwordx4 v[142:145], v[142:143], off
	v_mfma_f32_32x32x16_bf16 v[34:49], v[158:161], v[194:197], v[34:49]
	ds_read_b128 v[146:149], v218 offset:17968
	v_mfma_f32_32x32x16_bf16 v[18:33], v[162:165], v[186:189], v[18:33]
	ds_read_b64_tr_b16 v[178:179], v220
	ds_read_b64_tr_b16 v[180:181], v220 offset:2304
	v_mfma_f32_32x32x16_bf16 v[2:17], v[162:165], v[194:197], v[2:17]
	s_waitcnt lgkmcnt(10)
	v_mfma_f32_32x32x16_bf16 v[82:97], v[166:169], v[182:185], v[82:97]
	ds_read_b128 v[154:157], v218 offset:20528
	ds_read_b64_tr_b16 v[194:195], v221 offset:64
	ds_read_b64_tr_b16 v[196:197], v221 offset:2368
	s_waitcnt lgkmcnt(3)
	s_barrier
	s_waitcnt vmcnt(15)
	v_cmp_ne_u32_e32 vcc, 0, v251
	s_nop 1
	v_cndmask_b32_e32 v250, v250, v234, vcc
	v_max_i32_e32 v236, 0, v250
	v_mov_b32_e32 v237, 0
	v_lshl_add_u64 v[236:237], v[236:237], 2, s[10:11]
	global_load_dword v235, v[236:237], off
	v_mfma_f32_32x32x16_bf16 v[66:81], v[166:169], v[190:193], v[66:81]
	ds_read_b128 v[158:161], v218 offset:30736
	v_mfma_f32_32x32x16_bf16 v[50:65], v[170:173], v[182:185], v[50:65]
	v_mfma_f32_32x32x16_bf16 v[34:49], v[170:173], v[190:193], v[34:49]
	ds_read_b128 v[162:165], v218 offset:33296
	v_mfma_f32_32x32x16_bf16 v[18:33], v[174:177], v[182:185], v[18:33]
	ds_read_b64_tr_b16 v[182:183], v223
	ds_read_b64_tr_b16 v[184:185], v223 offset:2304
	v_mfma_f32_32x32x16_bf16 v[2:17], v[174:177], v[190:193], v[2:17]
	ds_read_b128 v[166:169], v218 offset:35856
	ds_read_b64_tr_b16 v[186:187], v223 offset:64
	ds_read_b64_tr_b16 v[188:189], v223 offset:2368
	v_mfma_f32_32x32x16_bf16 v[82:97], v[150:153], v[178:181], v[82:97]
	s_waitcnt vmcnt(10)
	ds_write_b128 v214, v[106:109] offset:16
	s_and_saveexec_b64 s[12:13], s[4:5]
	ds_write_b128 v215, v[98:101] offset:10256
	s_or_b64 exec, exec, s[12:13]
	s_waitcnt lgkmcnt(9)
	v_mfma_f32_32x32x16_bf16 v[66:81], v[150:153], v[194:197], v[66:81]
	ds_read_b128 v[170:173], v218 offset:30768
	s_waitcnt vmcnt(9)
	v_cvt_pk_bf16_f32 v150, v118, v119
	v_cvt_pk_bf16_f32 v151, v120, v121
	s_waitcnt vmcnt(8)
	v_cvt_pk_bf16_f32 v152, v110, v111
	v_cvt_pk_bf16_f32 v153, v112, v113
	ds_write2_b64 v198, v[150:151], v[152:153] offset0:130 offset1:202
	s_waitcnt vmcnt(7)
	v_cvt_pk_bf16_f32 v150, v114, v115
	v_cvt_pk_bf16_f32 v151, v116, v117
	s_waitcnt vmcnt(6)
	v_cvt_pk_bf16_f32 v152, v122, v123
	v_cvt_pk_bf16_f32 v153, v124, v125
	ds_write2_b64 v209, v[150:151], v[152:153] offset0:18 offset1:90
	v_mfma_f32_32x32x16_bf16 v[50:65], v[146:149], v[178:181], v[50:65]
	v_mfma_f32_32x32x16_bf16 v[34:49], v[146:149], v[194:197], v[34:49]
	ds_read_b128 v[174:177], v218 offset:33328
	v_mfma_f32_32x32x16_bf16 v[18:33], v[154:157], v[178:181], v[18:33]
	ds_read_b64_tr_b16 v[178:179], v224
	ds_read_b64_tr_b16 v[180:181], v224 offset:2304
	v_mfma_f32_32x32x16_bf16 v[2:17], v[154:157], v[194:197], v[2:17]
	s_waitcnt lgkmcnt(10)
	v_mfma_f32_32x32x16_bf16 v[82:97], v[158:161], v[182:185], v[82:97]
	ds_read_b128 v[190:193], v218 offset:35888
	ds_read_b64_tr_b16 v[194:195], v225 offset:64
	ds_read_b64_tr_b16 v[196:197], v225 offset:2368
	s_waitcnt lgkmcnt(3)
	s_barrier
; __device__ __forceinline__ void moe_unit(const int* pre, const int* lpre, int x, int lb, int& e, int& rb) {
;     if (lb < lpre[32]) {
;         int lo = 0, hi = 32;
;         while (hi - lo > 1) { const int mid = (lo + hi) >> 1; if (lpre[mid] <= lb) lo = mid; else hi = mid; }
;         e = x + 8 * lo; rb = lb - lpre[lo];
;     } else { e = 256; rb = (lb - lpre[32]) * 8 + x; }
; }
	v_mfma_f32_32x32x16_bf16 v[66:81], v[158:161], v[186:189], v[66:81]
	ds_read_b128 v[154:157], v218 offset:16
	v_mfma_f32_32x32x16_bf16 v[50:65], v[162:165], v[182:185], v[50:65]
	v_mfma_f32_32x32x16_bf16 v[34:49], v[162:165], v[186:189], v[34:49]
	ds_read_b128 v[158:161], v218 offset:2576
	v_mfma_f32_32x32x16_bf16 v[18:33], v[166:169], v[182:185], v[18:33]
	ds_read_b64_tr_b16 v[162:163], v226 offset:46096
	ds_read_b64_tr_b16 v[164:165], v226 offset:48400
	v_mfma_f32_32x32x16_bf16 v[2:17], v[166:169], v[186:189], v[2:17]
	ds_read_b128 v[146:149], v218 offset:5136
	ds_read_b64_tr_b16 v[150:151], v226 offset:46160
	ds_read_b64_tr_b16 v[152:153], v226 offset:48464
	v_mfma_f32_32x32x16_bf16 v[82:97], v[170:173], v[178:181], v[82:97]
	s_waitcnt vmcnt(5)
	ds_write_b128 v214, v[126:129] offset:15376
	s_and_saveexec_b64 s[12:13], s[4:5]
	ds_write_b128 v215, v[102:105] offset:25616
	s_or_b64 exec, exec, s[12:13]
	s_waitcnt lgkmcnt(9)
	v_mfma_f32_32x32x16_bf16 v[66:81], v[170:173], v[194:197], v[66:81]
	ds_read_b128 v[166:169], v218 offset:48
	s_waitcnt vmcnt(4)
	v_cvt_pk_bf16_f32 v170, v130, v131
	v_cvt_pk_bf16_f32 v171, v132, v133
	s_waitcnt vmcnt(3)
	v_cvt_pk_bf16_f32 v172, v134, v135
	v_cvt_pk_bf16_f32 v173, v136, v137
	ds_write2_b64 v217, v[170:171], v[172:173] offset1:72
	s_waitcnt vmcnt(2)
	v_cvt_pk_bf16_f32 v170, v138, v139
	v_cvt_pk_bf16_f32 v171, v140, v141
	s_waitcnt vmcnt(1)
	v_cvt_pk_bf16_f32 v172, v142, v143
	v_cvt_pk_bf16_f32 v173, v144, v145
	ds_write2_b64 v217, v[170:171], v[172:173] offset0:144 offset1:216
	v_mfma_f32_32x32x16_bf16 v[50:65], v[174:177], v[178:181], v[50:65]
	v_mfma_f32_32x32x16_bf16 v[34:49], v[174:177], v[194:197], v[34:49]
	ds_read_b128 v[170:173], v218 offset:2608
	v_mfma_f32_32x32x16_bf16 v[18:33], v[190:193], v[178:181], v[18:33]
	ds_read_b64_tr_b16 v[174:175], v226 offset:55312
	ds_read_b64_tr_b16 v[176:177], v226 offset:57616
	v_mfma_f32_32x32x16_bf16 v[2:17], v[190:193], v[194:197], v[2:17]
	s_waitcnt lgkmcnt(10)
	v_mfma_f32_32x32x16_bf16 v[82:97], v[154:157], v[162:165], v[82:97]
	ds_read_b128 v[178:181], v218 offset:5168
	ds_read_b64_tr_b16 v[182:183], v226 offset:55376
	ds_read_b64_tr_b16 v[184:185], v226 offset:57680
	s_waitcnt lgkmcnt(3)
	s_barrier
	v_mfma_f32_32x32x16_bf16 v[66:81], v[154:157], v[150:153], v[66:81]
	ds_read_b128 v[154:157], v218 offset:15376
	v_mfma_f32_32x32x16_bf16 v[50:65], v[158:161], v[162:165], v[50:65]
	v_mfma_f32_32x32x16_bf16 v[34:49], v[158:161], v[150:153], v[34:49]
	ds_read_b128 v[158:161], v218 offset:17936
	v_mfma_f32_32x32x16_bf16 v[18:33], v[146:149], v[162:165], v[18:33]
	ds_read_b64_tr_b16 v[162:163], v219
	ds_read_b64_tr_b16 v[164:165], v219 offset:2304
	v_mfma_f32_32x32x16_bf16 v[2:17], v[146:149], v[150:153], v[2:17]
	ds_read_b128 v[146:149], v218 offset:20496
	ds_read_b64_tr_b16 v[150:151], v219 offset:64
	ds_read_b64_tr_b16 v[152:153], v219 offset:2368
	v_mfma_f32_32x32x16_bf16 v[82:97], v[166:169], v[174:177], v[82:97]
	s_waitcnt lgkmcnt(7)
	v_mfma_f32_32x32x16_bf16 v[66:81], v[166:169], v[182:185], v[66:81]
	ds_read_b128 v[166:169], v218 offset:15408
	v_mfma_f32_32x32x16_bf16 v[50:65], v[170:173], v[174:177], v[50:65]
	v_mfma_f32_32x32x16_bf16 v[34:49], v[170:173], v[182:185], v[34:49]
	ds_read_b128 v[170:173], v218 offset:17968
	v_mfma_f32_32x32x16_bf16 v[18:33], v[178:181], v[174:177], v[18:33]
	ds_read_b64_tr_b16 v[174:175], v220
	ds_read_b64_tr_b16 v[176:177], v220 offset:2304
	v_mfma_f32_32x32x16_bf16 v[2:17], v[178:181], v[182:185], v[2:17]
	s_waitcnt lgkmcnt(7)
	v_mfma_f32_32x32x16_bf16 v[82:97], v[154:157], v[162:165], v[82:97]
	ds_read_b128 v[178:181], v218 offset:20528
	ds_read_b64_tr_b16 v[182:183], v221 offset:64
	ds_read_b64_tr_b16 v[184:185], v221 offset:2368
	s_waitcnt lgkmcnt(3)
	s_barrier
	v_mfma_f32_32x32x16_bf16 v[66:81], v[154:157], v[150:153], v[66:81]
	v_mfma_f32_32x32x16_bf16 v[50:65], v[158:161], v[162:165], v[50:65]
	v_mfma_f32_32x32x16_bf16 v[34:49], v[158:161], v[150:153], v[34:49]
	v_mfma_f32_32x32x16_bf16 v[18:33], v[146:149], v[162:165], v[18:33]
	v_mfma_f32_32x32x16_bf16 v[2:17], v[146:149], v[150:153], v[2:17]
	v_mfma_f32_32x32x16_bf16 v[82:97], v[166:169], v[174:177], v[82:97]
	s_waitcnt lgkmcnt(0)
	v_mfma_f32_32x32x16_bf16 v[66:81], v[166:169], v[182:185], v[66:81]
	v_mfma_f32_32x32x16_bf16 v[50:65], v[170:173], v[174:177], v[50:65]
	v_mfma_f32_32x32x16_bf16 v[34:49], v[170:173], v[182:185], v[34:49]
	v_mfma_f32_32x32x16_bf16 v[18:33], v[178:181], v[174:177], v[18:33]
	v_mfma_f32_32x32x16_bf16 v[2:17], v[178:181], v[182:185], v[2:17]
	s_add_i32 s23, s23, s27
	s_cmp_ge_i32 s23, s24
	s_cselect_b64 s[12:13], -1, 0
	s_and_b64 vcc, exec, s[12:13]
	s_barrier
	s_cbranch_vccnz .LBB0_2755
	s_mov_b32 s14, s68
	v_mov_b32_e32 v108, v238
